# v5: P12 gains hoisted; K-loop LDS-DMA saddr addressing; s_sleep 1 before the vmcnt wait in P10 load segments
# baseline (speedup 1.0000x reference)
; #define PG8_STAGE(bufoff, gbase, voff) do { _Pragma("unroll") for (int _i = 0; _i < 2; ++_i) \
;         __builtin_amdgcn_global_load_lds((const unsigned*)((const char*)(gbase) + (voff)[_i]), (LAS unsigned*)(lds + (bufoff) + ldsw + _i * 8192), 16, 0, 0); } while (0)
; #define PG8_WAIT_V(n) asm volatile("s_waitcnt vmcnt(" #n ")" ::: "memory")
; #define PG8_WAIT_L(n) asm volatile("s_waitcnt lgkmcnt(" #n ")" ::: "memory")
; #define PG8_BAR __builtin_amdgcn_s_barrier()
; template <bool GATHER, bool F8, class Epi, class Sched>
; __device__ __forceinline__ void gemm_phase(LAS unsigned char* lds, const int nt, const unsigned lda, const unsigned ldb, const Sched& S, const Epi& E) {
;     ...
;         for (int t = 0; t < nt; t += 2) {
;             const bool last = (t == nt - 2);
;             const char* a1 = cA + (size_t)(t + 1) * kstep;
;             const char* a2 = last ? nA : cA + (size_t)(t + 2) * kstep; const char* b2 = last ? nB : cB + (size_t)(t + 2) * kstep;
;             const char* a3 = a2 + kstep; const char* b3 = b2 + kstep;
;             unsigned w0[2], w1[2];
;             if constexpr (GATHER) {
; #pragma unroll
;                 for (int i = 0; i < 2; ++i) { w0[i] = last ? vN0[i] : vA0[i]; w1[i] = last ? vN1[i] : vA1[i]; }
;             } else {
; #pragma unroll
;                 for (int i = 0; i < 2; ++i) { w0[i] = voffA[i]; w1[i] = voffA[i]; }
;             }
;             PG8_LDB(B0, 0, 0); PG8_LDB(B1, 0, 1); PG8_SCHED; PG8_LDA(At, 0, 0); PG8_STAGE(PG8_SA(1, 1), a1 + hA, vA1);
;             PG8_WAIT_V(8); PG8_WAIT_L(0); PG8_BAR; PG8_MMA(0, 0, At, B0); PG8_MMA(0, 1, At, B1); PG8_BAR; PG8_SCHED;
;             PG8_LDA(At, 0, 1); PG8_STAGE(PG8_SB(0, 0), b2, voffB); PG8_STAGE(PG8_SB(0, 1), b2 + hB, voffB); PG8_STAGE(PG8_SA(0, 0), a2, w0);
;             PG8_WAIT_V(8); PG8_WAIT_L(0); PG8_BAR; PG8_MMA(1, 0, At, B0); PG8_MMA(1, 1, At, B1); PG8_BAR; PG8_SCHED;
;             PG8_LDB(B0, 1, 0); PG8_LDB(B1, 1, 1); PG8_SCHED; PG8_LDA(At, 1, 0); PG8_STAGE(PG8_SA(0, 1), a2 + hA, w1);
;             PG8_WAIT_V(8); PG8_WAIT_L(0); PG8_BAR; PG8_MMA(0, 0, At, B0); PG8_MMA(0, 1, At, B1); PG8_BAR; PG8_SCHED;
;             PG8_LDA(At, 1, 1); PG8_STAGE(PG8_SB(1, 0), b3, voffB); PG8_STAGE(PG8_SB(1, 1), b3 + hB, voffB); PG8_STAGE(PG8_SA(1, 0), a3, w0);
;             PG8_WAIT_V(8); PG8_WAIT_L(0); PG8_BAR; PG8_MMA(1, 0, At, B0); PG8_MMA(1, 1, At, B1); PG8_BAR; PG8_SCHED;
.Lp10_not_last:
	s_and_b64 s[34:35], vcc, exec
	v_cndmask_b32_e32 v164, v209, v208, vcc
	s_cselect_b32 s37, s23, s37
	s_cselect_b32 s36, s22, s36
	v_cndmask_b32_e32 v173, v172, v205, vcc
	v_cndmask_b32_e32 v242, v170, v207, vcc
	v_cndmask_b32_e32 v175, v174, v206, vcc
	s_cselect_b32 s35, s25, s68
	s_cselect_b32 s34, s24, s67
	s_add_i32 m0, s40, 0xbf80
	ds_read_b128 v[180:183], v202
	ds_read_b128 v[184:187], v202 offset:1024
	ds_read_b128 v[210:213], v202 offset:2048
	ds_read_b128 v[214:217], v202 offset:3072
	ds_read_b128 v[218:221], v202 offset:4096
	ds_read_b128 v[222:225], v202 offset:5120
	ds_read_b128 v[226:229], v202 offset:6144
	ds_read_b128 v[230:233], v202 offset:7168
	global_load_lds_dwordx4 v172, s[100:101] offset:128
	s_add_i32 m0, s40, 0xdf80
	s_nop 0
	global_load_lds_dwordx4 v174, s[100:101] offset:128
	s_sleep 1
	s_waitcnt vmcnt(8)
	s_waitcnt lgkmcnt(0)
	s_barrier
	s_setprio 1
	s_waitcnt lgkmcnt(0)
	v_mfma_scale_f32_16x16x128_f8f6f4 v[158:161], v[18:25], v[180:187], v[158:161], v203, v203 op_sel_hi:[0,0,0]
	v_mfma_scale_f32_16x16x128_f8f6f4 v[150:153], v[26:33], v[180:187], v[150:153], v203, v203 op_sel_hi:[0,0,0]
	v_mfma_scale_f32_16x16x128_f8f6f4 v[142:145], v[18:25], v[210:217], v[142:145], v203, v203 op_sel_hi:[0,0,0]
	v_mfma_scale_f32_16x16x128_f8f6f4 v[134:137], v[26:33], v[210:217], v[134:137], v203, v203 op_sel_hi:[0,0,0]
	v_mfma_scale_f32_16x16x128_f8f6f4 v[126:129], v[18:25], v[218:225], v[126:129], v203, v203 op_sel_hi:[0,0,0]
	v_mfma_scale_f32_16x16x128_f8f6f4 v[118:121], v[26:33], v[218:225], v[118:121], v203, v203 op_sel_hi:[0,0,0]
	v_mfma_scale_f32_16x16x128_f8f6f4 v[110:113], v[18:25], v[226:233], v[110:113], v203, v203 op_sel_hi:[0,0,0]
	v_mfma_scale_f32_16x16x128_f8f6f4 v[102:105], v[26:33], v[226:233], v[102:105], v203, v203 op_sel_hi:[0,0,0]
	s_setprio 0
	s_setprio 1
	v_mfma_scale_f32_16x16x128_f8f6f4 v[154:157], v[2:9], v[180:187], v[154:157], v203, v203 op_sel_hi:[0,0,0]
	v_mfma_scale_f32_16x16x128_f8f6f4 v[146:149], v[10:17], v[180:187], v[146:149], v203, v203 op_sel_hi:[0,0,0]
	v_mfma_scale_f32_16x16x128_f8f6f4 v[138:141], v[2:9], v[210:217], v[138:141], v203, v203 op_sel_hi:[0,0,0]
	v_mfma_scale_f32_16x16x128_f8f6f4 v[130:133], v[10:17], v[210:217], v[130:133], v203, v203 op_sel_hi:[0,0,0]
	v_mfma_scale_f32_16x16x128_f8f6f4 v[122:125], v[2:9], v[218:225], v[122:125], v203, v203 op_sel_hi:[0,0,0]
	v_mfma_scale_f32_16x16x128_f8f6f4 v[114:117], v[10:17], v[218:225], v[114:117], v203, v203 op_sel_hi:[0,0,0]
	v_mfma_scale_f32_16x16x128_f8f6f4 v[106:109], v[2:9], v[226:233], v[106:109], v203, v203 op_sel_hi:[0,0,0]
	v_mfma_scale_f32_16x16x128_f8f6f4 v[98:101], v[10:17], v[226:233], v[98:101], v203, v203 op_sel_hi:[0,0,0]
	s_setprio 0
	s_barrier
	s_mov_b32 m0, s41
	s_add_u32 s68, s34, 0x40000
	ds_read_b128 v[210:213], v202 offset:16384
	ds_read_b128 v[214:217], v202 offset:17408
	ds_read_b128 v[218:221], v202 offset:18432
	ds_read_b128 v[222:225], v202 offset:19456
	ds_read_b128 v[226:229], v202 offset:20480
	ds_read_b128 v[230:233], v202 offset:21504
	ds_read_b128 v[234:237], v202 offset:22528
	ds_read_b128 v[238:241], v202 offset:23552
	global_load_lds_dwordx4 v166, s[34:35]
	s_mov_b32 m0, s42
	s_addc_u32 s69, s35, 0
	global_load_lds_dwordx4 v168, s[34:35]
	s_mov_b32 m0, s43
	s_nop 0
	global_load_lds_dwordx4 v166, s[68:69]
	s_mov_b32 m0, s44
	s_nop 0
	global_load_lds_dwordx4 v168, s[68:69]
	s_mov_b32 m0, s40
	s_nop 0
	global_load_lds_dwordx4 v164, s[36:37]
	s_mov_b32 m0, s45
	s_nop 0
	global_load_lds_dwordx4 v242, s[36:37]
	s_sleep 1
	s_waitcnt vmcnt(8)
	s_waitcnt lgkmcnt(0)
	s_barrier
	s_setprio 1
	s_waitcnt lgkmcnt(0)
	v_mfma_scale_f32_16x16x128_f8f6f4 v[94:97], v[18:25], v[210:217], v[94:97], v203, v203 op_sel_hi:[0,0,0]
	v_mfma_scale_f32_16x16x128_f8f6f4 v[86:89], v[26:33], v[210:217], v[86:89], v203, v203 op_sel_hi:[0,0,0]
	v_mfma_scale_f32_16x16x128_f8f6f4 v[78:81], v[18:25], v[218:225], v[78:81], v203, v203 op_sel_hi:[0,0,0]
	v_mfma_scale_f32_16x16x128_f8f6f4 v[70:73], v[26:33], v[218:225], v[70:73], v203, v203 op_sel_hi:[0,0,0]
	v_mfma_scale_f32_16x16x128_f8f6f4 v[54:57], v[18:25], v[226:233], v[54:57], v203, v203 op_sel_hi:[0,0,0]
	v_mfma_scale_f32_16x16x128_f8f6f4 v[50:53], v[26:33], v[226:233], v[50:53], v203, v203 op_sel_hi:[0,0,0]
	v_mfma_scale_f32_16x16x128_f8f6f4 v[38:41], v[18:25], v[234:241], v[38:41], v203, v203 op_sel_hi:[0,0,0]
	v_mfma_scale_f32_16x16x128_f8f6f4 v[34:37], v[26:33], v[234:241], v[34:37], v203, v203 op_sel_hi:[0,0,0]
	s_setprio 0
	s_setprio 1
	v_mfma_scale_f32_16x16x128_f8f6f4 v[90:93], v[2:9], v[210:217], v[90:93], v203, v203 op_sel_hi:[0,0,0]
	v_mfma_scale_f32_16x16x128_f8f6f4 v[82:85], v[10:17], v[210:217], v[82:85], v203, v203 op_sel_hi:[0,0,0]
	v_mfma_scale_f32_16x16x128_f8f6f4 v[74:77], v[2:9], v[218:225], v[74:77], v203, v203 op_sel_hi:[0,0,0]
	v_mfma_scale_f32_16x16x128_f8f6f4 v[62:65], v[10:17], v[218:225], v[62:65], v203, v203 op_sel_hi:[0,0,0]
	v_mfma_scale_f32_16x16x128_f8f6f4 v[66:69], v[2:9], v[226:233], v[66:69], v203, v203 op_sel_hi:[0,0,0]
	v_mfma_scale_f32_16x16x128_f8f6f4 v[58:61], v[10:17], v[226:233], v[58:61], v203, v203 op_sel_hi:[0,0,0]
	v_mfma_scale_f32_16x16x128_f8f6f4 v[46:49], v[2:9], v[234:241], v[46:49], v203, v203 op_sel_hi:[0,0,0]
	v_mfma_scale_f32_16x16x128_f8f6f4 v[42:45], v[10:17], v[234:241], v[42:45], v203, v203 op_sel_hi:[0,0,0]
	s_setprio 0
	s_barrier
; #define PG8_STAGE(bufoff, gbase, voff) do { _Pragma("unroll") for (int _i = 0; _i < 2; ++_i) \
;         __builtin_amdgcn_global_load_lds((const unsigned*)((const char*)(gbase) + (voff)[_i]), (LAS unsigned*)(lds + (bufoff) + ldsw + _i * 8192), 16, 0, 0); } while (0)
; #define PG8_LDA(dst, b, h) do { if constexpr (F8) { _Pragma("unroll") for (int m = 0; m < 4; ++m) dst##8[m] = PG8_LD8(lds, PG8_SA(b, h) + aoff + m * 2048); } \
;         else { _Pragma("unroll") for (int m = 0; m < 4; ++m) _Pragma("unroll") for (int k = 0; k < 2; ++k) dst[m][k] = *(const LAS bf16x8*)(lds + PG8_SA(b, h) + aoff + m * 2048 + k * 1024); } } while (0)
; #define PG8_LDB(dst, b, h) do { if constexpr (F8) { _Pragma("unroll") for (int n = 0; n < 2; ++n) dst##8[n] = PG8_LD8(ldsB, PG8_SBR(b, h) + boff + n * 2048); } \
;         else { _Pragma("unroll") for (int n = 0; n < 2; ++n) _Pragma("unroll") for (int k = 0; k < 2; ++k) dst[n][k] = *(const LAS bf16x8*)(ldsB + PG8_SBR(b, h) + boff + n * 2048 + k * 1024); } } while (0)
; #define PG8_WAIT_V(n) asm volatile("s_waitcnt vmcnt(" #n ")" ::: "memory")
; #define PG8_WAIT_L(n) asm volatile("s_waitcnt lgkmcnt(" #n ")" ::: "memory")
; #define PG8_BAR __builtin_amdgcn_s_barrier()
; #define PG8_SCHED __builtin_amdgcn_sched_barrier(0)
; template <bool GATHER, bool F8, class Epi, class Sched>
; __device__ __forceinline__ void gemm_phase(LAS unsigned char* lds, const int nt, const unsigned lda, const unsigned ldb, const Sched& S, const Epi& E) {
;     ...
;             PG8_LDB(B0, 1, 0); PG8_LDB(B1, 1, 1); PG8_SCHED; PG8_LDA(At, 1, 0); PG8_STAGE(PG8_SA(0, 1), a2 + hA, w1);
;             PG8_WAIT_V(8); PG8_WAIT_L(0); PG8_BAR; PG8_MMA(0, 0, At, B0); PG8_MMA(0, 1, At, B1); PG8_BAR; PG8_SCHED;
;             PG8_LDA(At, 1, 1); PG8_STAGE(PG8_SB(1, 0), b3, voffB); PG8_STAGE(PG8_SB(1, 1), b3 + hB, voffB); PG8_STAGE(PG8_SA(1, 0), a3, w0);
;             PG8_WAIT_V(8); PG8_WAIT_L(0); PG8_BAR; PG8_MMA(1, 0, At, B0); PG8_MMA(1, 1, At, B1); PG8_BAR; PG8_SCHED;
;         }
;         if (wr == 0) PG8_BAR;
	ds_read_b128 v[2:5], v201 offset:32768
	ds_read_b128 v[6:9], v201 offset:33792
	ds_read_b128 v[10:13], v201 offset:34816
	ds_read_b128 v[14:17], v201 offset:35840
	ds_read_b128 v[18:21], v201 offset:49152
	ds_read_b128 v[22:25], v201 offset:50176
	ds_read_b128 v[26:29], v201 offset:51200
	ds_read_b128 v[30:33], v201 offset:52224
	s_mov_b32 m0, s46
	ds_read_b128 v[210:213], v202 offset:32768
	ds_read_b128 v[214:217], v202 offset:33792
	ds_read_b128 v[218:221], v202 offset:34816
	ds_read_b128 v[222:225], v202 offset:35840
	ds_read_b128 v[226:229], v202 offset:36864
	ds_read_b128 v[230:233], v202 offset:37888
	ds_read_b128 v[234:237], v202 offset:38912
	ds_read_b128 v[238:241], v202 offset:39936
	global_load_lds_dwordx4 v173, s[36:37]
	s_mov_b32 m0, s47
	s_nop 0
	global_load_lds_dwordx4 v175, s[36:37]
	s_sleep 1
	s_waitcnt vmcnt(8)
	s_waitcnt lgkmcnt(0)
	s_barrier
	s_setprio 1
	s_waitcnt lgkmcnt(0)
	v_mfma_scale_f32_16x16x128_f8f6f4 v[158:161], v[2:9], v[210:217], v[158:161], v203, v203 op_sel_hi:[0,0,0]
	v_mfma_scale_f32_16x16x128_f8f6f4 v[150:153], v[10:17], v[210:217], v[150:153], v203, v203 op_sel_hi:[0,0,0]
	v_mfma_scale_f32_16x16x128_f8f6f4 v[142:145], v[2:9], v[218:225], v[142:145], v203, v203 op_sel_hi:[0,0,0]
	v_mfma_scale_f32_16x16x128_f8f6f4 v[134:137], v[10:17], v[218:225], v[134:137], v203, v203 op_sel_hi:[0,0,0]
	v_mfma_scale_f32_16x16x128_f8f6f4 v[126:129], v[2:9], v[226:233], v[126:129], v203, v203 op_sel_hi:[0,0,0]
	v_mfma_scale_f32_16x16x128_f8f6f4 v[118:121], v[10:17], v[226:233], v[118:121], v203, v203 op_sel_hi:[0,0,0]
	v_mfma_scale_f32_16x16x128_f8f6f4 v[110:113], v[2:9], v[234:241], v[110:113], v203, v203 op_sel_hi:[0,0,0]
	v_mfma_scale_f32_16x16x128_f8f6f4 v[102:105], v[10:17], v[234:241], v[102:105], v203, v203 op_sel_hi:[0,0,0]
	s_setprio 0
	s_setprio 1
	v_mfma_scale_f32_16x16x128_f8f6f4 v[154:157], v[18:25], v[210:217], v[154:157], v203, v203 op_sel_hi:[0,0,0]
	v_mfma_scale_f32_16x16x128_f8f6f4 v[146:149], v[26:33], v[210:217], v[146:149], v203, v203 op_sel_hi:[0,0,0]
	v_mfma_scale_f32_16x16x128_f8f6f4 v[138:141], v[18:25], v[218:225], v[138:141], v203, v203 op_sel_hi:[0,0,0]
	v_mfma_scale_f32_16x16x128_f8f6f4 v[130:133], v[26:33], v[218:225], v[130:133], v203, v203 op_sel_hi:[0,0,0]
	v_mfma_scale_f32_16x16x128_f8f6f4 v[122:125], v[18:25], v[226:233], v[122:125], v203, v203 op_sel_hi:[0,0,0]
	v_mfma_scale_f32_16x16x128_f8f6f4 v[114:117], v[26:33], v[226:233], v[114:117], v203, v203 op_sel_hi:[0,0,0]
	v_mfma_scale_f32_16x16x128_f8f6f4 v[106:109], v[18:25], v[234:241], v[106:109], v203, v203 op_sel_hi:[0,0,0]
	v_mfma_scale_f32_16x16x128_f8f6f4 v[98:101], v[26:33], v[234:241], v[98:101], v203, v203 op_sel_hi:[0,0,0]
	s_setprio 0
	s_barrier
	s_add_i32 m0, s50, 0xffffff80
	ds_read_b128 v[210:213], v202 offset:49152
	ds_read_b128 v[214:217], v202 offset:50176
	ds_read_b128 v[218:221], v202 offset:51200
	ds_read_b128 v[222:225], v202 offset:52224
	ds_read_b128 v[226:229], v202 offset:53248
	ds_read_b128 v[230:233], v202 offset:54272
	ds_read_b128 v[234:237], v202 offset:55296
	ds_read_b128 v[238:241], v202 offset:56320
	global_load_lds_dwordx4 v166, s[34:35] offset:128
	s_add_i32 m0, s51, 0xffffff80
	s_nop 0
	global_load_lds_dwordx4 v168, s[34:35] offset:128
	s_add_u32 s34, s34, 0x40080
	s_addc_u32 s35, s35, 0
	s_mov_b32 m0, s54
	s_nop 0
	global_load_lds_dwordx4 v166, s[34:35]
	s_mov_b32 m0, s55
	s_nop 0
	global_load_lds_dwordx4 v168, s[34:35]
	s_add_i32 m0, s52, 0xffffff80
	s_nop 0
	global_load_lds_dwordx4 v164, s[36:37] offset:128
	s_add_i32 m0, s53, 0xffffff80
	s_nop 0
	global_load_lds_dwordx4 v242, s[36:37] offset:128
	s_sleep 1
	s_waitcnt vmcnt(8)
	s_waitcnt lgkmcnt(0)
	s_barrier
	s_setprio 1
	s_waitcnt lgkmcnt(0)
	v_mfma_scale_f32_16x16x128_f8f6f4 v[94:97], v[2:9], v[210:217], v[94:97], v203, v203 op_sel_hi:[0,0,0]
	v_mfma_scale_f32_16x16x128_f8f6f4 v[86:89], v[10:17], v[210:217], v[86:89], v203, v203 op_sel_hi:[0,0,0]
	v_mfma_scale_f32_16x16x128_f8f6f4 v[78:81], v[2:9], v[218:225], v[78:81], v203, v203 op_sel_hi:[0,0,0]
	v_mfma_scale_f32_16x16x128_f8f6f4 v[70:73], v[10:17], v[218:225], v[70:73], v203, v203 op_sel_hi:[0,0,0]
	v_mfma_scale_f32_16x16x128_f8f6f4 v[54:57], v[2:9], v[226:233], v[54:57], v203, v203 op_sel_hi:[0,0,0]
	v_mfma_scale_f32_16x16x128_f8f6f4 v[50:53], v[10:17], v[226:233], v[50:53], v203, v203 op_sel_hi:[0,0,0]
	v_mfma_scale_f32_16x16x128_f8f6f4 v[38:41], v[2:9], v[234:241], v[38:41], v203, v203 op_sel_hi:[0,0,0]
	v_mfma_scale_f32_16x16x128_f8f6f4 v[34:37], v[10:17], v[234:241], v[34:37], v203, v203 op_sel_hi:[0,0,0]
	s_setprio 0
	s_setprio 1
	v_mfma_scale_f32_16x16x128_f8f6f4 v[90:93], v[18:25], v[210:217], v[90:93], v203, v203 op_sel_hi:[0,0,0]
	v_mfma_scale_f32_16x16x128_f8f6f4 v[82:85], v[26:33], v[210:217], v[82:85], v203, v203 op_sel_hi:[0,0,0]
	v_mfma_scale_f32_16x16x128_f8f6f4 v[74:77], v[18:25], v[218:225], v[74:77], v203, v203 op_sel_hi:[0,0,0]
	v_mfma_scale_f32_16x16x128_f8f6f4 v[62:65], v[26:33], v[218:225], v[62:65], v203, v203 op_sel_hi:[0,0,0]
	v_mfma_scale_f32_16x16x128_f8f6f4 v[66:69], v[18:25], v[226:233], v[66:69], v203, v203 op_sel_hi:[0,0,0]
	v_mfma_scale_f32_16x16x128_f8f6f4 v[58:61], v[26:33], v[226:233], v[58:61], v203, v203 op_sel_hi:[0,0,0]
	v_mfma_scale_f32_16x16x128_f8f6f4 v[46:49], v[18:25], v[234:241], v[46:49], v203, v203 op_sel_hi:[0,0,0]
	v_mfma_scale_f32_16x16x128_f8f6f4 v[42:45], v[26:33], v[234:241], v[42:45], v203, v203 op_sel_hi:[0,0,0]
	s_setprio 0
	s_barrier
	s_add_i32 s39, s39, 2
	s_add_u32 s0, s0, 0x100
	s_addc_u32 s1, s1, 0
	s_cmp_gt_u32 s39, 13
	s_cbranch_scc0 .LBB0_1927
	s_and_b64 vcc, exec, s[12:13]
	s_cbranch_vccz .LBB0_1930
	s_barrier
